# attention main loop: the step's K and V LDS-DMA pieces issued at the head of the step (right behind the mask-word load) instead of after the QK MFMAs and row-max tree
# speedup vs baseline: 1.0085x; 1.0047x over previous
.LBB0_1273:
	s_movk_i32 s42, 0xff00
	s_mov_b32 s43, -1
	v_lshl_add_u64 v[86:87], v[192:193], 0, s[42:43]
	global_load_dword v2, v[86:87], off
	v_lshl_add_u64 v[222:223], v[188:189], 0, s[86:87]
	s_add_i32 s63, s47, s58
	s_mov_b32 m0, s63
	s_nop 0
	global_load_lds_dwordx4 v[222:223], off
	v_lshl_add_u64 v[222:223], v[190:191], 0, s[86:87]
	s_add_i32 s63, s48, s59
	s_mov_b32 m0, s63
	s_nop 0
	global_load_lds_dwordx4 v[222:223], off
	v_add_u32_e32 v255, s4, v220
	ds_read_b64_tr_b16 v[182:183], v255 offset:24576
	ds_read_b64_tr_b16 v[184:185], v255 offset:25088
	s_waitcnt lgkmcnt(9)
	v_mfma_f32_32x32x16_bf16 v[102:117], v[178:181], v[138:141], v[36:51]
	v_cvt_pk_bf16_f32 v146, v68, v69
	v_cvt_pk_bf16_f32 v147, v70, v71
	ds_read_b64_tr_b16 v[178:179], v255 offset:28672
	ds_read_b64_tr_b16 v[180:181], v255 offset:29184
	s_waitcnt lgkmcnt(10)
	v_mfma_f32_32x32x16_bf16 v[86:101], v[170:173], v[138:141], v[36:51]
	v_cvt_pk_bf16_f32 v148, v72, v73
	v_cvt_pk_bf16_f32 v149, v74, v75
	ds_read_b64_tr_b16 v[170:171], v255 offset:25600
	ds_read_b64_tr_b16 v[172:173], v255 offset:26112
	s_waitcnt lgkmcnt(11)
	v_mfma_f32_32x32x16_bf16 v[102:117], v[174:177], v[134:137], v[102:117]
	v_cvt_pk_bf16_f32 v142, v76, v77
	v_cvt_pk_bf16_f32 v143, v78, v79
	ds_read_b64_tr_b16 v[76:77], v255 offset:29696
	ds_read_b64_tr_b16 v[78:79], v255 offset:30208
	s_waitcnt lgkmcnt(12)
	v_mfma_f32_32x32x16_bf16 v[86:101], v[162:165], v[134:137], v[86:101]
	v_cvt_pk_bf16_f32 v144, v80, v81
	v_cvt_pk_bf16_f32 v145, v82, v83
	ds_read_b64_tr_b16 v[72:73], v255 offset:26624
	ds_read_b64_tr_b16 v[74:75], v255 offset:27136
	s_waitcnt lgkmcnt(13)
	v_mfma_f32_32x32x16_bf16 v[102:117], v[166:169], v[126:129], v[102:117]
	v_cvt_pk_bf16_f32 v130, v52, v53
	v_cvt_pk_bf16_f32 v131, v54, v55
	ds_read_b64_tr_b16 v[68:69], v255 offset:30720
	ds_read_b64_tr_b16 v[70:71], v255 offset:31232
	s_waitcnt lgkmcnt(14)
	v_mfma_f32_32x32x16_bf16 v[86:101], v[154:157], v[126:129], v[86:101]
	v_cvt_pk_bf16_f32 v132, v56, v57
	v_cvt_pk_bf16_f32 v133, v58, v59
	ds_read_b64_tr_b16 v[56:57], v255 offset:27648
	ds_read_b64_tr_b16 v[58:59], v255 offset:28160
	s_waitcnt lgkmcnt(14)
	v_mfma_f32_32x32x16_bf16 v[102:117], v[158:161], v[122:125], v[102:117]
	v_cvt_pk_bf16_f32 v118, v60, v61
	v_cvt_pk_bf16_f32 v119, v62, v63
	ds_read_b64_tr_b16 v[52:53], v255 offset:31744
	ds_read_b64_tr_b16 v[54:55], v255 offset:32256
	v_mfma_f32_32x32x16_bf16 v[86:101], v[150:153], v[122:125], v[86:101]
	v_cvt_pk_bf16_f32 v120, v64, v65
	v_cvt_pk_bf16_f32 v121, v66, v67
	ds_read_b128 v[80:83], v225 offset:51200
	v_max_f32_e32 v60, v103, v103
	v_max_f32_e32 v61, v102, v102
	v_max_f32_e32 v60, v61, v60
	v_max3_f32 v61, v104, v105, v87
	v_max3_f32 v60, v60, v86, v88
	v_max3_f32 v60, v60, v89, v106
	v_max3_f32 v61, v61, v108, v109
	v_max3_f32 v60, v60, v107, v90
	v_max3_f32 v61, v61, v92, v93
	v_max3_f32 v60, v60, v91, v110
	v_max3_f32 v61, v61, v112, v113
	v_max3_f32 v60, v60, v111, v94
	v_max3_f32 v61, v61, v96, v97
	v_max3_f32 v60, v60, v95, v114
	v_max3_f32 v61, v61, v116, v117
	v_max3_f32 v60, v60, v115, v98
	v_max3_f32 v61, v61, v100, v101
	v_max3_f32 v60, v60, v99, v61
	v_mov_b32_e32 v61, v60
	s_nop 1
	v_permlane32_swap_b32_e32 v60, v61
	v_max_f32_e32 v61, v61, v61
	v_max_f32_e32 v60, v60, v60
	v_max_f32_e32 v60, v60, v61
	v_cmp_lt_f32_e32 vcc, s14, v60
	s_cmp_lg_u64 vcc, 0
	s_cselect_b64 s[42:43], -1, 0
	s_cbranch_vccnz .LBB0_1281

; #define WAIT_BAR(N) asm volatile("s_waitcnt vmcnt(" #N ") lgkmcnt(0)\n\ts_barrier":::"memory")
;   #define RESC() do{ if(resc){ asm volatile("s_waitcnt lgkmcnt(0)":::"memory"); \
;       _Pragma("unroll") for(int d_=0;d_<2;++d_) _Pragma("unroll") for(int r=0;r<16;++r)o[d_][r]*=wsf[crow(r,hi)]; } }while(0)
;   #define ROT() do{sl_prev=sl_cur;sl_cur=sl_next;sl_next=(sl_next==(NSLOT-1)*SLOTB)?0:sl_next+SLOTB;}while(0)
; template<int THRL> __device__ __forceinline__ void attn_unit(int b,int h,int qb,const bf16*Q,const bf16*__restrict__ K,const bf16*__restrict__ V,bf16*O,const unsigned*MASK,char*shm){
;     ...
;     STEP(pA0,pA1,pB0,pB1,t+1,true,true,true,wA,wB);   WAIT_BAR(2); RESC(); ROT();
.LBB0_1276:
	s_add_i32 s4, s48, 0x2000
	s_cmpk_lg_i32 s48, 0x4000
	s_cselect_b32 s60, s4, 0
	global_load_dword v218, v[192:193], off
	s_add_i32 s63, s48, s58
	s_mov_b32 m0, s63
	s_nop 0
	global_load_lds_dwordx4 v[188:189], off
	s_add_i32 s63, s60, s59
	s_mov_b32 m0, s63
	s_nop 0
	global_load_lds_dwordx4 v[190:191], off
	v_add_u32_e32 v255, s47, v220
	ds_read_b64_tr_b16 v[182:183], v255 offset:24576
	ds_read_b64_tr_b16 v[184:185], v255 offset:25088
	s_waitcnt lgkmcnt(9)
	v_mfma_f32_32x32x16_bf16 v[68:83], v[60:63], v[138:141], v[36:51]
	v_cvt_pk_bf16_f32 v146, v102, v103
	v_cvt_pk_bf16_f32 v147, v104, v105
	ds_read_b64_tr_b16 v[178:179], v255 offset:28672
	ds_read_b64_tr_b16 v[180:181], v255 offset:29184
	s_waitcnt lgkmcnt(10)
	v_mfma_f32_32x32x16_bf16 v[52:67], v[150:153], v[138:141], v[36:51]
	v_cvt_pk_bf16_f32 v148, v106, v107
	v_cvt_pk_bf16_f32 v149, v108, v109
	ds_read_b64_tr_b16 v[150:151], v255 offset:25600
	ds_read_b64_tr_b16 v[152:153], v255 offset:26112
	s_waitcnt lgkmcnt(11)
	v_mfma_f32_32x32x16_bf16 v[68:83], v[174:177], v[134:137], v[68:83]
	v_cvt_pk_bf16_f32 v142, v110, v111
	v_cvt_pk_bf16_f32 v143, v112, v113
	ds_read_b64_tr_b16 v[110:111], v255 offset:29696
	ds_read_b64_tr_b16 v[112:113], v255 offset:30208
	s_waitcnt lgkmcnt(12)
	v_mfma_f32_32x32x16_bf16 v[52:67], v[162:165], v[134:137], v[52:67]
	v_cvt_pk_bf16_f32 v144, v114, v115
	v_cvt_pk_bf16_f32 v145, v116, v117
	ds_read_b64_tr_b16 v[106:107], v255 offset:26624
	ds_read_b64_tr_b16 v[108:109], v255 offset:27136
	s_waitcnt lgkmcnt(13)
	v_mfma_f32_32x32x16_bf16 v[68:83], v[170:173], v[126:129], v[68:83]
	v_cvt_pk_bf16_f32 v130, v86, v87
	v_cvt_pk_bf16_f32 v131, v88, v89
	ds_read_b64_tr_b16 v[102:103], v255 offset:30720
	ds_read_b64_tr_b16 v[104:105], v255 offset:31232
	s_waitcnt lgkmcnt(14)
	v_mfma_f32_32x32x16_bf16 v[52:67], v[158:161], v[126:129], v[52:67]
	v_cvt_pk_bf16_f32 v132, v90, v91
	v_cvt_pk_bf16_f32 v133, v92, v93
	ds_read_b64_tr_b16 v[90:91], v255 offset:27648
	ds_read_b64_tr_b16 v[92:93], v255 offset:28160
	s_waitcnt lgkmcnt(14)
	v_mfma_f32_32x32x16_bf16 v[68:83], v[166:169], v[122:125], v[68:83]
	v_cvt_pk_bf16_f32 v118, v94, v95
	v_cvt_pk_bf16_f32 v119, v96, v97
	ds_read_b64_tr_b16 v[86:87], v255 offset:31744
	ds_read_b64_tr_b16 v[88:89], v255 offset:32256
	v_mfma_f32_32x32x16_bf16 v[52:67], v[154:157], v[122:125], v[52:67]
	v_cvt_pk_bf16_f32 v120, v98, v99
	v_cvt_pk_bf16_f32 v121, v100, v101
	ds_read_b128 v[114:117], v225 offset:51200
	v_max_f32_e32 v95, v69, v69
	v_max_f32_e32 v96, v68, v68
	v_max_f32_e32 v95, v96, v95
	s_nop 3
	v_max3_f32 v96, v70, v71, v53
	v_max3_f32 v95, v95, v52, v54
	v_max3_f32 v95, v95, v55, v72
	v_max3_f32 v96, v96, v74, v75
	v_max3_f32 v95, v95, v73, v56
	v_max3_f32 v96, v96, v58, v59
	v_max3_f32 v95, v95, v57, v76
	v_max3_f32 v96, v96, v78, v79
	v_max3_f32 v95, v95, v77, v60
	v_max3_f32 v96, v96, v62, v63
	v_max3_f32 v95, v95, v61, v80
	v_max3_f32 v96, v96, v82, v83
	v_max3_f32 v95, v95, v81, v64
	v_max3_f32 v96, v96, v66, v67
	v_max3_f32 v94, v95, v65, v96
	v_mov_b32_e32 v95, v94
	s_nop 1
	v_permlane32_swap_b32_e32 v94, v95
	v_max_f32_e32 v95, v95, v95
	v_max_f32_e32 v94, v94, v94
	v_max_f32_e32 v94, v94, v95
	v_cmp_lt_f32_e32 vcc, s14, v94
	s_cmp_lg_u64 vcc, 0
	s_cselect_b64 s[42:43], -1, 0
	s_cbranch_vccnz .LBB0_1284
